# speedup vs baseline: 1.0046x; 1.0046x over previous
.Lp_w1t:
	s_sleep 30
	s_load_dwordx2 s[16:17], s[0:1], 0x38
	s_load_dwordx2 s[18:19], s[0:1], 0x40
	s_load_dwordx4 s[20:23], s[0:1], 0x48
	v_lshl_or_b32 v2, s2, 8, v0
	v_add_u32_e32 v2, 0xfffec000, v2
	v_mov_b32_e32 v3, 0
	v_mov_b32_e32 v26, v0
	v_lshrrev_b32_e32 v4, 3, v2
	v_lshrrev_b32_e32 v5, 3, v0
	v_lshlrev_b32_e32 v0, 1, v0
	v_and_b32_e32 v4, 0x1fffffe0, v4
	v_and_b32_e32 v6, 0x80, v0
	v_mov_b32_e32 v7, 0
	v_and_or_b32 v4, v5, 20, v4
	s_waitcnt lgkmcnt(0)
	v_lshl_add_u64 v[8:9], s[8:9], 0, v[6:7]
	v_lshlrev_b32_e32 v6, 2, v1
	v_lshl_add_u64 v[0:1], v[8:9], 0, v[6:7]
	v_or_b32_e32 v6, 1, v4
	v_lshlrev_b64 v[10:11], 8, v[6:7]
	v_or_b32_e32 v6, 2, v4
	v_lshlrev_b64 v[12:13], 8, v[6:7]
	v_or_b32_e32 v6, 3, v4
	v_lshlrev_b64 v[14:15], 8, v[6:7]
	v_or_b32_e32 v6, 8, v4
	v_lshlrev_b64 v[16:17], 8, v[6:7]
	v_or_b32_e32 v6, 9, v4
	v_mov_b32_e32 v5, v7
	v_lshlrev_b64 v[18:19], 8, v[6:7]
	v_or_b32_e32 v6, 10, v4
	v_lshlrev_b64 v[8:9], 8, v[4:5]
	v_lshlrev_b64 v[20:21], 8, v[6:7]
	v_or_b32_e32 v6, 11, v4
	v_lshl_add_u64 v[8:9], v[0:1], 0, v[8:9]
	v_lshlrev_b64 v[4:5], 8, v[6:7]
	v_lshl_add_u64 v[10:11], v[0:1], 0, v[10:11]
	v_lshl_add_u64 v[12:13], v[0:1], 0, v[12:13]
	v_lshl_add_u64 v[14:15], v[0:1], 0, v[14:15]
	v_lshl_add_u64 v[16:17], v[0:1], 0, v[16:17]
	v_lshl_add_u64 v[18:19], v[0:1], 0, v[18:19]
	v_lshl_add_u64 v[20:21], v[0:1], 0, v[20:21]
	v_lshl_add_u64 v[0:1], v[0:1], 0, v[4:5]
	global_load_dword v4, v[8:9], off
	global_load_dword v5, v[10:11], off
	global_load_dword v6, v[12:13], off
	global_load_dword v7, v[14:15], off
	global_load_dword v22, v[16:17], off
	global_load_dword v23, v[18:19], off
	global_load_dword v24, v[20:21], off
	global_load_dword v25, v[0:1], off
	v_lshl_add_u64 v[0:1], v[2:3], 4, s[16:17]
	s_getpc_b64 s[24:25]
	s_and_b32 s24, s24, 0xfffff000
	v_lshlrev_b32_e32 v32, 7, v26
	v_mov_b32_e32 v33, 0
	v_lshl_add_u64 v[34:35], s[24:25], 0, v[32:33]
	global_load_dword v31, v[34:35], off sc0 sc1
	v_add_co_u32_e32 v38, vcc, 0xffffe000, v34
	s_nop 1
	v_addc_co_u32_e32 v39, vcc, -1, v35, vcc
	global_load_dword v27, v[38:39], off sc0 sc1
	s_waitcnt vmcnt(2)
	v_cvt_pk_f16_f32 v4, v4, v5
	v_cvt_pk_f16_f32 v5, v6, v7
	v_cvt_pk_f16_f32 v6, v22, v23
	v_cvt_pk_f16_f32 v7, v24, v25
	global_store_dwordx4 v[0:1], v[4:7], off sc1
	s_movk_i32 s4, 0x70
	v_cmp_gt_u32_e32 vcc, s4, v26
	s_and_saveexec_b64 s[4:5], vcc
	s_cbranch_execz .Lp_t1
	v_add_co_u32_e32 v34, vcc, 0x8000, v34
	s_nop 1
	v_addc_co_u32_e32 v35, vcc, 0, v35, vcc
	global_load_dword v8, v[34:35], off sc0 sc1
